# nt cache hint on the fully-coalesced producer stores of the elementwise phases (h1 in phase 1, sub-LN and conv outputs in phase 4, h2 in phase 8) so less dirty L2 is left for the barrier write-back; o
# baseline (speedup 1.0000x reference)
; __device__ __forceinline__ float dot4(f32x4 a, f32x4 b) { return (a.x * b.x + a.y * b.y) + (a.z * b.z + a.w * b.w); }
; __device__ __forceinline__ void phase1(KP kp, LAS unsigned char* lds, int wave, int bid, int G) {
;     ...
;         f32x4 v[8]; float s = 0.f;
; #pragma unroll
;         for (int j = 0; j < 8; ++j) { v[j] = xr[64 * j]; s += dot4(v[j], v[j]); }
;         const float rstd = 1.0f / sqrtf(wave_sum(s) * (1.0f / DM) + EPS);
.Lp1row_nopf:
	v_mul_f32_e32 v131, v64, v64
	v_pk_mul_f32 v[84:85], v[70:71], v[70:71]
	v_pk_mul_f32 v[110:111], v[68:69], v[68:69]
	v_mul_f32_e32 v112, v77, v77
	v_mul_f32_e32 v114, v79, v79
	v_mul_f32_e32 v129, v74, v74
	v_mul_f32_e32 v137, v75, v75
	v_pk_mov_b32 v[116:117], v[110:111], v[84:85] op_sel:[1,0]
	v_mov_b32_e32 v111, v85
	v_pk_fma_f32 v[84:85], v[76:77], v[76:77], v[112:113] op_sel_hi:[1,1,0]
	v_pk_fma_f32 v[112:113], v[78:79], v[78:79], v[114:115] op_sel_hi:[1,1,0]
	v_mov_b32_e32 v118, v95
	v_mov_b32_e32 v119, v99
	v_mov_b32_e32 v122, v97
	v_mov_b32_e32 v123, v101
	v_mov_b32_e32 v114, v94
	v_mov_b32_e32 v115, v98
	v_mov_b32_e32 v120, v96
	v_mov_b32_e32 v121, v100
	v_pk_mul_f32 v[124:125], v[104:105], v[104:105]
	v_pk_mul_f32 v[126:127], v[102:103], v[102:103]
	v_pk_add_f32 v[110:111], v[116:117], v[110:111]
	v_mov_b32_e32 v85, v129
	v_mov_b32_e32 v113, v137
	v_pk_mul_f32 v[116:117], v[118:119], v[118:119]
	v_pk_mul_f32 v[118:119], v[122:123], v[122:123]
	v_pk_mov_b32 v[122:123], v[126:127], v[124:125] op_sel:[1,0]
	v_mov_b32_e32 v127, v125
	v_pk_add_f32 v[84:85], v[84:85], v[112:113]
	v_pk_fma_f32 v[112:113], v[114:115], v[114:115], v[116:117]
	v_pk_fma_f32 v[114:115], v[120:121], v[120:121], v[118:119]
	v_mul_f32_e32 v128, v107, v107
	v_mul_f32_e32 v130, v109, v109
	v_pk_add_f32 v[116:117], v[122:123], v[126:127]
	v_pk_add_f32 v[112:113], v[112:113], v[114:115]
	v_mul_f32_e32 v132, v65, v65
	v_mul_f32_e32 v133, v66, v66
	v_mul_f32_e32 v134, v67, v67
	v_pk_fma_f32 v[124:125], v[106:107], v[106:107], v[128:129] op_sel_hi:[1,1,0]
	v_pk_fma_f32 v[128:129], v[108:109], v[108:109], v[130:131] op_sel_hi:[1,1,0]
	v_pk_add_f32 v[114:115], v[116:117], v[116:117] op_sel:[0,1] op_sel_hi:[1,0]
	v_pk_add_f32 v[112:113], v[112:113], v[112:113] op_sel:[0,1] op_sel_hi:[1,0]
	v_mov_b32_e32 v125, v133
	v_mov_b32_e32 v129, v134
	v_mov_b32_e32 v115, v132
	v_mov_b32_e32 v113, v131
	v_pk_add_f32 v[116:117], v[124:125], v[128:129]
	v_pk_add_f32 v[112:113], v[112:113], v[114:115]
	v_mul_f32_e32 v135, v72, v72
	v_pk_add_f32 v[112:113], v[112:113], v[116:117]
	v_mul_f32_e32 v136, v73, v73
	v_pk_add_f32 v[110:111], v[110:111], v[110:111] op_sel:[0,1] op_sel_hi:[1,0]
	v_pk_add_f32 v[112:113], v[112:113], v[112:113] op_sel:[0,1] op_sel_hi:[1,0]
	v_mov_b32_e32 v111, v136
	v_mov_b32_e32 v113, v135
	v_pk_add_f32 v[110:111], v[112:113], v[110:111]
	s_nop 0
	v_pk_add_f32 v[84:85], v[110:111], v[84:85]
	s_nop 0
	v_add_f32_e32 v84, v84, v85
	s_nop 1
	v_add_f32_dpp v84, v84, v84 quad_perm:[1,0,3,2] row_mask:0xf bank_mask:0xf
	s_nop 1
	v_add_f32_dpp v84, v84, v84 quad_perm:[2,3,0,1] row_mask:0xf bank_mask:0xf
	s_nop 1
	v_add_f32_dpp v84, v84, v84 row_half_mirror row_mask:0xf bank_mask:0xf
	s_nop 1
	v_add_f32_dpp v84, v84, v84 row_mirror row_mask:0xf bank_mask:0xf
	v_mov_b32_e32 v85, v84
	s_nop 1
	v_permlane16_swap_b32_e32 v84, v85
	v_add_f32_e32 v84, v84, v85
	v_mov_b32_e32 v85, v84
	s_nop 1
	v_permlane32_swap_b32_e32 v84, v85
	v_add_f32_e32 v84, v84, v85
	v_fmamk_f32 v84, v84, 0x3a000000, v92
	v_mul_f32_e32 v85, 0x4f800000, v84
	v_cmp_gt_f32_e32 vcc, s4, v84
	s_nop 1
	v_cndmask_b32_e32 v84, v84, v85, vcc
	v_sqrt_f32_e32 v85, v84
	s_nop 0
	v_add_u32_e32 v110, -1, v85
	v_add_u32_e32 v111, 1, v85
	v_fma_f32 v112, -v110, v85, v84
	v_fma_f32 v113, -v111, v85, v84
	v_cmp_ge_f32_e64 s[2:3], 0, v112
	s_nop 1
	v_cndmask_b32_e64 v85, v85, v110, s[2:3]
	v_cmp_lt_f32_e64 s[2:3], 0, v113
	s_nop 1
	v_cndmask_b32_e64 v85, v85, v111, s[2:3]
	v_mul_f32_e32 v110, 0x37800000, v85
	v_cndmask_b32_e32 v85, v85, v110, vcc
	v_cmp_class_f32_e32 vcc, v84, v93
	s_nop 1
	v_cndmask_b32_e32 v84, v85, v84, vcc
	v_div_scale_f32 v85, s[2:3], v84, v84, 1.0
	v_rcp_f32_e32 v111, v85
	v_div_scale_f32 v110, vcc, 1.0, v84, 1.0
	v_fma_f32 v112, -v85, v111, 1.0
	v_fmac_f32_e32 v111, v112, v111
	v_mul_f32_e32 v112, v110, v111
	v_fma_f32 v113, -v85, v112, v110
	v_fmac_f32_e32 v112, v113, v111
	v_fma_f32 v85, -v85, v112, v110
	v_div_fmas_f32 v85, v85, v111, v112
	v_div_fixup_f32 v84, v85, v84, 1.0
	v_pk_mul_f32 v[94:95], v[94:95], v[84:85] op_sel_hi:[1,0]
	v_pk_mul_f32 v[96:97], v[96:97], v[84:85] op_sel_hi:[1,0]
	v_pk_mul_f32 v[98:99], v[98:99], v[84:85] op_sel_hi:[1,0]
	v_pk_mul_f32 v[100:101], v[100:101], v[84:85] op_sel_hi:[1,0]
	v_pk_mul_f32 v[102:103], v[102:103], v[84:85] op_sel_hi:[1,0]
	v_pk_mul_f32 v[104:105], v[104:105], v[84:85] op_sel_hi:[1,0]
	v_pk_mul_f32 v[106:107], v[106:107], v[84:85] op_sel_hi:[1,0]
	v_pk_mul_f32 v[108:109], v[108:109], v[84:85] op_sel_hi:[1,0]
	v_pk_mul_f32 v[64:65], v[64:65], v[84:85] op_sel_hi:[1,0]
	v_pk_mul_f32 v[66:67], v[66:67], v[84:85] op_sel_hi:[1,0]
	v_pk_mul_f32 v[68:69], v[68:69], v[84:85] op_sel_hi:[1,0]
; #define GAS __attribute__((address_space(1)))
; #define LAS __attribute__((address_space(3)))
; __device__ __forceinline__ u32x2 pack4(f32x4 v) { u32x2 w; w.x = pk2(v.x, v.y); w.y = pk2(v.z, v.w); return w; }
; __device__ __forceinline__ unsigned f2bf(float f) { unsigned u = __builtin_bit_cast(unsigned, f); return (u + 0x7fffu + ((u >> 16) & 1u)) >> 16; }
; __device__ __forceinline__ unsigned pk2(float lo, float hi) { return f2bf(lo) | (f2bf(hi) << 16); }
; __device__ __forceinline__ void phase1(KP kp, LAS unsigned char* lds, int wave, int bid, int G) {
;     ...
;         GAS u32x2* o8 = (GAS u32x2*)(H + (size_t)m * DM) + lane;
; #pragma unroll
;         for (int j = 0; j < 8; ++j) { const f32x4 av = *(const LAS f32x4*)(A1 + 256 * j + 4 * lane), bv = *(const LAS f32x4*)(B1 + 256 * j + 4 * lane);
;             o8[64 * j] = pack4(v[j] * rstd * av + bv); }
	v_pk_mul_f32 v[70:71], v[70:71], v[84:85] op_sel_hi:[1,0]
	v_pk_mul_f32 v[76:77], v[76:77], v[84:85] op_sel_hi:[1,0]
	v_pk_mul_f32 v[78:79], v[78:79], v[84:85] op_sel_hi:[1,0]
	v_pk_mul_f32 v[72:73], v[72:73], v[84:85] op_sel_hi:[1,0]
	v_pk_mul_f32 v[74:75], v[74:75], v[84:85] op_sel_hi:[1,0]
	v_pk_fma_f32 v[84:85], v[2:3], v[96:97], v[10:11]
	v_pk_fma_f32 v[94:95], v[0:1], v[94:95], v[8:9]
	v_pk_fma_f32 v[96:97], v[6:7], v[100:101], v[14:15]
	v_pk_fma_f32 v[98:99], v[4:5], v[98:99], v[12:13]
	v_pk_fma_f32 v[100:101], v[18:19], v[104:105], v[26:27]
	v_pk_fma_f32 v[102:103], v[16:17], v[102:103], v[24:25]
	v_pk_fma_f32 v[104:105], v[22:23], v[108:109], v[30:31]
	v_pk_fma_f32 v[106:107], v[20:21], v[106:107], v[28:29]
	v_pk_fma_f32 v[66:67], v[34:35], v[66:67], v[42:43]
	v_pk_fma_f32 v[64:65], v[32:33], v[64:65], v[40:41]
	v_pk_fma_f32 v[70:71], v[38:39], v[70:71], v[46:47]
	v_pk_fma_f32 v[68:69], v[36:37], v[68:69], v[44:45]
	v_pk_fma_f32 v[78:79], v[50:51], v[78:79], v[58:59]
	v_pk_fma_f32 v[76:77], v[48:49], v[76:77], v[56:57]
	v_pk_fma_f32 v[74:75], v[54:55], v[74:75], v[62:63]
	v_pk_fma_f32 v[72:73], v[52:53], v[72:73], v[60:61]
	v_bfe_u32 v108, v94, 16, 1
	v_bfe_u32 v110, v84, 16, 1
	v_bfe_u32 v109, v95, 16, 1
	v_bfe_u32 v111, v85, 16, 1
	v_bfe_u32 v112, v98, 16, 1
	v_bfe_u32 v114, v96, 16, 1
	v_bfe_u32 v116, v102, 16, 1
	v_bfe_u32 v118, v100, 16, 1
	v_bfe_u32 v120, v106, 16, 1
	v_bfe_u32 v122, v104, 16, 1
	v_bfe_u32 v124, v64, 16, 1
	v_bfe_u32 v125, v65, 16, 1
	v_bfe_u32 v126, v66, 16, 1
	v_bfe_u32 v127, v67, 16, 1
	v_bfe_u32 v128, v68, 16, 1
	v_bfe_u32 v129, v69, 16, 1
	v_bfe_u32 v130, v70, 16, 1
	v_bfe_u32 v131, v71, 16, 1
	v_bfe_u32 v132, v76, 16, 1
	v_bfe_u32 v134, v78, 16, 1
	v_bfe_u32 v136, v72, 16, 1
	v_bfe_u32 v137, v73, 16, 1
	v_bfe_u32 v138, v74, 16, 1
	v_add3_u32 v94, v94, v108, s5
	v_add3_u32 v84, v84, v110, s5
	v_bfe_u32 v113, v99, 16, 1
	v_bfe_u32 v115, v97, 16, 1
	v_bfe_u32 v117, v103, 16, 1
	v_bfe_u32 v119, v101, 16, 1
	v_bfe_u32 v121, v107, 16, 1
	v_bfe_u32 v123, v105, 16, 1
	v_bfe_u32 v133, v77, 16, 1
	v_bfe_u32 v135, v79, 16, 1
	v_bfe_u32 v139, v75, 16, 1
	v_add3_u32 v95, v95, v109, s5
	v_add3_u32 v85, v85, v111, s5
	v_add3_u32 v98, v98, v112, s5
	v_add3_u32 v96, v96, v114, s5
	v_add3_u32 v102, v102, v116, s5
	v_add3_u32 v100, v100, v118, s5
	v_add3_u32 v106, v106, v120, s5
	v_add3_u32 v104, v104, v122, s5
	v_add3_u32 v64, v64, v124, s5
	v_add3_u32 v108, v65, v125, s5
	v_add3_u32 v65, v66, v126, s5
	v_add3_u32 v109, v67, v127, s5
	v_add3_u32 v66, v68, v128, s5
	v_add3_u32 v110, v69, v129, s5
	v_add3_u32 v67, v70, v130, s5
	v_add3_u32 v111, v71, v131, s5
	v_add3_u32 v68, v76, v132, s5
	v_add3_u32 v69, v78, v134, s5
	v_add3_u32 v70, v72, v136, s5
	v_add3_u32 v78, v73, v137, s5
	v_add3_u32 v71, v74, v138, s5
	v_lshrrev_b32_e32 v72, 16, v94
	v_lshrrev_b32_e32 v73, 16, v84
	v_add3_u32 v99, v99, v113, s5
	v_add3_u32 v97, v97, v115, s5
	v_add3_u32 v103, v103, v117, s5
	v_add3_u32 v101, v101, v119, s5
	v_add3_u32 v107, v107, v121, s5
	v_add3_u32 v105, v105, v123, s5
	v_add3_u32 v76, v77, v133, s5
	v_add3_u32 v77, v79, v135, s5
	v_add3_u32 v79, v75, v139, s5
	v_lshrrev_b32_e32 v74, 16, v98
	v_lshrrev_b32_e32 v75, 16, v96
	v_lshrrev_b32_e32 v84, 16, v102
	v_lshrrev_b32_e32 v94, 16, v100
	v_lshrrev_b32_e32 v96, 16, v106
	v_lshrrev_b32_e32 v98, 16, v104
	v_lshrrev_b32_e32 v100, 16, v64
	v_lshrrev_b32_e32 v102, 16, v65
	v_lshrrev_b32_e32 v104, 16, v66
	v_lshrrev_b32_e32 v106, 16, v67
	v_lshrrev_b32_e32 v112, 16, v68
	v_lshrrev_b32_e32 v113, 16, v69
	v_lshrrev_b32_e32 v114, 16, v70
	v_lshrrev_b32_e32 v115, 16, v71
	v_and_or_b32 v64, v95, s9, v72
	v_and_or_b32 v65, v85, s9, v73
	v_and_or_b32 v66, v99, s9, v74
	v_and_or_b32 v67, v97, s9, v75
	v_and_or_b32 v68, v103, s9, v84
	v_and_or_b32 v69, v101, s9, v94
	v_and_or_b32 v70, v107, s9, v96
	v_and_or_b32 v71, v105, s9, v98
	v_and_or_b32 v72, v108, s9, v100
	v_and_or_b32 v73, v109, s9, v102
	v_and_or_b32 v74, v110, s9, v104
	v_and_or_b32 v75, v111, s9, v106
	v_and_or_b32 v76, v76, s9, v112
	v_and_or_b32 v77, v77, s9, v113
	v_and_or_b32 v78, v78, s9, v114
	v_and_or_b32 v79, v79, s9, v115
	global_store_dwordx2 v[80:81], v[64:65], off offset:-3584 nt
	global_store_dwordx2 v[80:81], v[66:67], off offset:-3072 nt
	global_store_dwordx2 v[80:81], v[68:69], off offset:-2560 nt
	global_store_dwordx2 v[80:81], v[70:71], off offset:-2048 nt
	global_store_dwordx2 v[80:81], v[72:73], off offset:-1536 nt
	global_store_dwordx2 v[80:81], v[74:75], off offset:-1024 nt
	global_store_dwordx2 v[80:81], v[76:77], off offset:-512 nt
	global_store_dwordx2 v[80:81], v[78:79], off nt
	v_lshl_add_u64 v[80:81], v[80:81], 0, s[6:7]
	s_cmpk_lt_i32 s8, 0x2000
	s_waitcnt vmcnt(8)
	s_cbranch_scc1 .Lp1row_loop

; #define GAS __attribute__((address_space(1)))
; __device__ __forceinline__ float dot4(f32x4 a, f32x4 b) { return (a.x * b.x + a.y * b.y) + (a.z * b.z + a.w * b.w); }
; __device__ __forceinline__ u32x2 pack4(f32x4 v) { u32x2 w; w.x = pk2(v.x, v.y); w.y = pk2(v.z, v.w); return w; }
; __device__ __forceinline__ f32x4 unpack4(u32x2 w) { return (f32x4){bflo(w.x), bfhi(w.x), bflo(w.y), bfhi(w.y)}; }
; __device__ __forceinline__ void phase4(KP kp, int wave, int bid, int G) {
;     ...
;     for (int it = gw; it < T * 8; it += NGW) { const int t = it >> 3, hd = it & 7;
;         const bf16* o0 = OA + (size_t)t * 4096 + hd * 512 + 4 * lane;
;         const f32x4 d = unpack4(*(const GAS u32x2*)o0) - lam * unpack4(*(const GAS u32x2*)(o0 + 256));
;         const float rstd = 1.0f / sqrtf(wave_sum(dot4(d, d)) * (1.0f / 256.0f) + EPS);
;         *(GAS u32x2*)(ON + (size_t)t * 4096 + hd * 256 + 4 * lane) = pack4(d * rstd * sg); }
.LBB0_709:
	s_ashr_i32 s2, s9, 3
	s_ashr_i32 s3, s2, 31
	s_lshl_b64 s[2:3], s[2:3], 13
	v_xor_b32_e32 v11, 0x80000000, v3
	v_lshl_add_u64 v[22:23], v[6:7], 0, s[2:3]
	s_lshl_b32 s24, s18, 1
	s_add_i32 s24, s24, s9
	s_min_i32 s24, s24, 0xffff
	s_ashr_i32 s22, s24, 3
	s_ashr_i32 s23, s22, 31
	s_lshl_b64 s[22:23], s[22:23], 13
	v_lshl_add_u64 v[60:61], v[4:5], 0, s[22:23]
	s_add_i32 s9, s9, s18
	s_waitcnt vmcnt(4)
	v_lshlrev_b32_e32 v28, 16, v56
	v_and_b32_e32 v29, 0xffff0000, v56
	v_lshlrev_b32_e32 v24, 16, v57
	v_and_b32_e32 v25, 0xffff0000, v57
	v_lshlrev_b32_e32 v30, 16, v58
	v_and_b32_e32 v31, 0xffff0000, v58
	v_lshlrev_b32_e32 v26, 16, v59
	v_and_b32_e32 v27, 0xffff0000, v59
	global_load_dwordx2 v[56:57], v[60:61], off nt
	global_load_dwordx2 v[58:59], v[60:61], off offset:512 nt
	v_pk_fma_f32 v[28:29], v[8:9], v[30:31], v[28:29] neg_lo:[1,0,0] neg_hi:[1,0,0]
	v_pk_fma_f32 v[24:25], v[10:11], v[26:27], v[24:25]
	v_pk_mul_f32 v[30:31], v[28:29], v[28:29]
	v_pk_mul_f32 v[26:27], v[24:25], v[24:25]
	s_nop 0
	v_pk_mov_b32 v[32:33], v[30:31], v[26:27] op_sel:[1,0]
	v_mov_b32_e32 v31, v27
	v_pk_add_f32 v[26:27], v[32:33], v[30:31]
	s_nop 0
	v_add_f32_e32 v11, v26, v27
	s_nop 1
	v_add_f32_dpp v11, v11, v11 quad_perm:[1,0,3,2] row_mask:0xf bank_mask:0xf
	s_nop 1
	v_add_f32_dpp v11, v11, v11 quad_perm:[2,3,0,1] row_mask:0xf bank_mask:0xf
	s_nop 1
	v_add_f32_dpp v11, v11, v11 row_half_mirror row_mask:0xf bank_mask:0xf
	s_nop 1
	v_add_f32_dpp v11, v11, v11 row_mirror row_mask:0xf bank_mask:0xf
	v_mov_b32_e32 v26, v11
	s_nop 1
	v_permlane16_swap_b32_e32 v11, v26
	v_add_f32_e32 v11, v11, v26
	v_mov_b32_e32 v26, v11
	s_nop 1
	v_permlane32_swap_b32_e32 v11, v26
	v_add_f32_e32 v11, v11, v26
	v_fmamk_f32 v11, v11, 0x3b800000, v20
	v_mul_f32_e32 v26, 0x4f800000, v11
	v_cmp_gt_f32_e32 vcc, s5, v11
	s_nop 1
	v_cndmask_b32_e32 v11, v11, v26, vcc
	v_sqrt_f32_e32 v26, v11
	s_nop 0
	v_add_u32_e32 v27, -1, v26
	v_add_u32_e32 v30, 1, v26
	v_fma_f32 v31, -v27, v26, v11
	v_fma_f32 v32, -v30, v26, v11
	v_cmp_ge_f32_e64 s[2:3], 0, v31
	s_nop 1
	v_cndmask_b32_e64 v26, v26, v27, s[2:3]
	v_cmp_lt_f32_e64 s[2:3], 0, v32
	s_nop 1
	v_cndmask_b32_e64 v26, v26, v30, s[2:3]
	v_mul_f32_e32 v27, 0x37800000, v26
	v_cndmask_b32_e32 v26, v26, v27, vcc
	v_cmp_class_f32_e32 vcc, v11, v21
	s_nop 1
	v_cndmask_b32_e32 v11, v26, v11, vcc
	v_div_scale_f32 v26, s[2:3], v11, v11, 1.0
	v_rcp_f32_e32 v30, v26
	v_div_scale_f32 v27, vcc, 1.0, v11, 1.0
	v_fma_f32 v31, -v26, v30, 1.0
	v_fmac_f32_e32 v30, v31, v30
	v_mul_f32_e32 v31, v27, v30
	v_fma_f32 v32, -v26, v31, v27
	v_fmac_f32_e32 v31, v32, v30
	v_fma_f32 v26, -v26, v31, v27
	v_div_fmas_f32 v26, v26, v30, v31
	v_div_fixup_f32 v26, v26, v11, 1.0
	v_pk_mul_f32 v[28:29], v[28:29], v[26:27] op_sel_hi:[1,0]
	v_pk_mul_f32 v[24:25], v[24:25], v[26:27] op_sel_hi:[1,0]
	v_pk_mul_f32 v[26:27], v[14:15], v[28:29]
	v_pk_mul_f32 v[24:25], v[12:13], v[24:25]
	v_bfe_u32 v11, v26, 16, 1
	v_bfe_u32 v29, v24, 16, 1
	v_bfe_u32 v28, v27, 16, 1
	v_bfe_u32 v30, v25, 16, 1
	v_add3_u32 v11, v26, v11, s8
	v_add3_u32 v24, v24, v29, s8
	v_add3_u32 v26, v27, v28, s8
	v_add3_u32 v25, v25, v30, s8
	v_lshrrev_b32_e32 v11, 16, v11
	v_lshrrev_b32_e32 v27, 16, v24
	v_and_or_b32 v24, v26, s4, v11
	v_and_or_b32 v25, v25, s4, v27
	global_store_dwordx2 v[22:23], v[24:25], off nt
	s_cmp_gt_i32 s9, 0xffff
	s_cbranch_scc1 .Lp4_exit
	s_ashr_i32 s2, s9, 3
	s_ashr_i32 s3, s2, 31
	s_lshl_b64 s[2:3], s[2:3], 13
	v_xor_b32_e32 v11, 0x80000000, v3
	v_lshl_add_u64 v[22:23], v[6:7], 0, s[2:3]
	s_lshl_b32 s24, s18, 1
	s_add_i32 s24, s24, s9
	s_min_i32 s24, s24, 0xffff
	s_ashr_i32 s22, s24, 3
	s_ashr_i32 s23, s22, 31
	s_lshl_b64 s[22:23], s[22:23], 13
	v_lshl_add_u64 v[60:61], v[4:5], 0, s[22:23]
	s_add_i32 s9, s9, s18
	s_waitcnt vmcnt(4)
	v_lshlrev_b32_e32 v28, 16, v62
	v_and_b32_e32 v29, 0xffff0000, v62
	v_lshlrev_b32_e32 v24, 16, v63
	v_and_b32_e32 v25, 0xffff0000, v63
	v_lshlrev_b32_e32 v30, 16, v64
	v_and_b32_e32 v31, 0xffff0000, v64
	v_lshlrev_b32_e32 v26, 16, v65
	v_and_b32_e32 v27, 0xffff0000, v65
	global_load_dwordx2 v[62:63], v[60:61], off nt
	global_load_dwordx2 v[64:65], v[60:61], off offset:512 nt
	v_pk_fma_f32 v[28:29], v[8:9], v[30:31], v[28:29] neg_lo:[1,0,0] neg_hi:[1,0,0]
	v_pk_fma_f32 v[24:25], v[10:11], v[26:27], v[24:25]
	v_pk_mul_f32 v[30:31], v[28:29], v[28:29]
	v_pk_mul_f32 v[26:27], v[24:25], v[24:25]
	s_nop 0
	v_pk_mov_b32 v[32:33], v[30:31], v[26:27] op_sel:[1,0]
	v_mov_b32_e32 v31, v27
	v_pk_add_f32 v[26:27], v[32:33], v[30:31]
	s_nop 0
	v_add_f32_e32 v11, v26, v27
	s_nop 1
	v_add_f32_dpp v11, v11, v11 quad_perm:[1,0,3,2] row_mask:0xf bank_mask:0xf
	s_nop 1
	v_add_f32_dpp v11, v11, v11 quad_perm:[2,3,0,1] row_mask:0xf bank_mask:0xf
	s_nop 1
	v_add_f32_dpp v11, v11, v11 row_half_mirror row_mask:0xf bank_mask:0xf
	s_nop 1
	v_add_f32_dpp v11, v11, v11 row_mirror row_mask:0xf bank_mask:0xf
	v_mov_b32_e32 v26, v11
	s_nop 1
	v_permlane16_swap_b32_e32 v11, v26
	v_add_f32_e32 v11, v11, v26
	v_mov_b32_e32 v26, v11
	s_nop 1
	v_permlane32_swap_b32_e32 v11, v26
	v_add_f32_e32 v11, v11, v26
	v_fmamk_f32 v11, v11, 0x3b800000, v20
	v_mul_f32_e32 v26, 0x4f800000, v11
	v_cmp_gt_f32_e32 vcc, s5, v11
	s_nop 1
	v_cndmask_b32_e32 v11, v11, v26, vcc
	v_sqrt_f32_e32 v26, v11
	s_nop 0
	v_add_u32_e32 v27, -1, v26
	v_add_u32_e32 v30, 1, v26
	v_fma_f32 v31, -v27, v26, v11
	v_fma_f32 v32, -v30, v26, v11
	v_cmp_ge_f32_e64 s[2:3], 0, v31
	s_nop 1
	v_cndmask_b32_e64 v26, v26, v27, s[2:3]
	v_cmp_lt_f32_e64 s[2:3], 0, v32
	s_nop 1
	v_cndmask_b32_e64 v26, v26, v30, s[2:3]
	v_mul_f32_e32 v27, 0x37800000, v26
	v_cndmask_b32_e32 v26, v26, v27, vcc
	v_cmp_class_f32_e32 vcc, v11, v21
	s_nop 1
	v_cndmask_b32_e32 v11, v26, v11, vcc
	v_div_scale_f32 v26, s[2:3], v11, v11, 1.0
	v_rcp_f32_e32 v30, v26
	v_div_scale_f32 v27, vcc, 1.0, v11, 1.0
	v_fma_f32 v31, -v26, v30, 1.0
	v_fmac_f32_e32 v30, v31, v30
	v_mul_f32_e32 v31, v27, v30
	v_fma_f32 v32, -v26, v31, v27
	v_fmac_f32_e32 v31, v32, v30
	v_fma_f32 v26, -v26, v31, v27
	v_div_fmas_f32 v26, v26, v30, v31
	v_div_fixup_f32 v26, v26, v11, 1.0
	v_pk_mul_f32 v[28:29], v[28:29], v[26:27] op_sel_hi:[1,0]
	v_pk_mul_f32 v[24:25], v[24:25], v[26:27] op_sel_hi:[1,0]
	v_pk_mul_f32 v[26:27], v[14:15], v[28:29]
	v_pk_mul_f32 v[24:25], v[12:13], v[24:25]
	v_bfe_u32 v11, v26, 16, 1
	v_bfe_u32 v29, v24, 16, 1
	v_bfe_u32 v28, v27, 16, 1
	v_bfe_u32 v30, v25, 16, 1
	v_add3_u32 v11, v26, v11, s8
	v_add3_u32 v24, v24, v29, s8
	v_add3_u32 v26, v27, v28, s8
	v_add3_u32 v25, v25, v30, s8
	v_lshrrev_b32_e32 v11, 16, v11
	v_lshrrev_b32_e32 v27, 16, v24
	v_and_or_b32 v24, v26, s4, v11
	v_and_or_b32 v25, v25, s4, v27
	global_store_dwordx2 v[22:23], v[24:25], off nt
	s_cmp_gt_i32 s9, 0xffff
	s_cbranch_scc0 .LBB0_709

; #define GAS __attribute__((address_space(1)))
; __device__ __forceinline__ u32x2 pack4(f32x4 v) { u32x2 w; w.x = pk2(v.x, v.y); w.y = pk2(v.z, v.w); return w; }
; __device__ __forceinline__ f32x4 unpack4(u32x2 w) { return (f32x4){bflo(w.x), bfhi(w.x), bflo(w.y), bfhi(w.y)}; }
; __device__ __forceinline__ void phase4(KP kp, int wave, int bid, int G) {
;     ...
;         for (int i = 0; i < 16; ++i) { const int t = t0 + i; const bf16* r = R + (size_t)t * 10240 + ch;
;             const v4u b = *(const GAS v4u*)r, c = *(const GAS v4u*)(r + 2048), h = *(const GAS v4u*)(r + 4096);
;             const f32x4 ua = unpack4((u32x2){c.x, c.y}) * unpack4((u32x2){h.x, h.y}), ub = unpack4((u32x2){c.z, c.w}) * unpack4((u32x2){h.z, h.w});
;             const f32x4 ya = unpack4((u32x2){b.x, b.y}) * (w0a * u2a + w1a * u1a + w2a * ua), yb = unpack4((u32x2){b.z, b.w}) * (w0b * u2b + w1b * u1b + w2b * ub);
;             const u32x2 pa = pack4(ya), pb = pack4(yb);
;             *(GAS v4u*)(CV + (size_t)t * 4096 + ch) = (v4u){pa.x, pa.y, pb.x, pb.y};
;             u2a = u1a; u2b = u1b; u1a = ua; u1b = ub; }
.LBB0_715:
	s_waitcnt vmcnt(4)
	v_pk_mul_f32 v[32:33], v[8:9], v[32:33]
	v_lshl_add_u64 v[2:3], s[14:15], 0, v[46:47]
	v_pk_mul_f32 v[60:61], v[8:9], v[36:37]
	s_waitcnt vmcnt(2)
	v_pk_fma_f32 v[68:69], v[16:17], v[36:37], v[32:33]
	v_add_co_u32_e64 v36, s[2:3], s29, v2
	v_lshl_add_u64 v[48:49], s[26:27], 0, v[46:47]
	v_pk_mul_f32 v[34:35], v[10:11], v[34:35]
	v_addc_co_u32_e64 v37, s[2:3], 0, v3, s[2:3]
	v_pk_fma_f32 v[66:67], v[18:19], v[38:39], v[34:35]
	v_add_co_u32_e64 v34, s[2:3], s30, v48
	v_pk_mul_f32 v[28:29], v[4:5], v[28:29]
	s_nop 0
	v_addc_co_u32_e64 v35, s[2:3], 0, v49, s[2:3]
	v_add_co_u32_e64 v72, s[2:3], s31, v48
	v_pk_fma_f32 v[70:71], v[12:13], v[40:41], v[28:29]
	s_nop 0
	v_addc_co_u32_e64 v73, s[2:3], 0, v49, s[2:3]
	v_add_co_u32_e64 v28, s[2:3], s34, v2
	v_pk_mul_f32 v[30:31], v[6:7], v[30:31]
	s_nop 0
	v_addc_co_u32_e64 v29, s[2:3], 0, v3, s[2:3]
	v_pk_mul_f32 v[62:63], v[6:7], v[42:43]
	v_pk_fma_f32 v[42:43], v[14:15], v[42:43], v[30:31]
	v_add_co_u32_e64 v30, s[2:3], s35, v48
	v_add_co_u32_e32 v50, vcc, 0x3e000000, v48
	s_nop 0
	v_addc_co_u32_e64 v31, s[2:3], 0, v49, s[2:3]
	v_add_co_u32_e64 v32, s[2:3], s36, v48
	v_addc_co_u32_e32 v51, vcc, 0, v49, vcc
	s_nop 0
	v_addc_co_u32_e64 v33, s[2:3], 0, v49, s[2:3]
	v_add_co_u32_e64 v74, s[2:3], s37, v2
	v_add_co_u32_e32 v52, vcc, 0x3e001000, v48
	s_nop 0
	v_addc_co_u32_e64 v75, s[2:3], 0, v3, s[2:3]
	v_add_co_u32_e64 v76, s[2:3], s38, v48
	v_addc_co_u32_e32 v53, vcc, 0, v49, vcc
	s_nop 0
	v_addc_co_u32_e64 v77, s[2:3], 0, v49, s[2:3]
	v_add_co_u32_e64 v78, s[2:3], s39, v48
	v_add_co_u32_e32 v48, vcc, 0x3e002000, v48
	s_nop 0
	v_addc_co_u32_e64 v79, s[2:3], 0, v49, s[2:3]
	v_addc_co_u32_e32 v49, vcc, 0, v49, vcc
	v_pk_mul_f32 v[58:59], v[10:11], v[38:39]
	v_pk_mul_f32 v[64:65], v[4:5], v[40:41]
	global_load_dwordx4 v[160:163], v[50:51], off nt
	global_load_dwordx4 v[164:167], v[48:49], off nt
	global_load_dwordx4 v[168:171], v[52:53], off nt
	global_load_dwordx4 v[172:175], v[34:35], off nt
	global_load_dwordx4 v[176:179], v[72:73], off nt
	global_load_dwordx4 v[180:183], v[34:35], off offset:-4096 nt
	global_load_dwordx4 v[184:187], v[30:31], off nt
	global_load_dwordx4 v[188:191], v[32:33], off nt
	global_load_dwordx4 v[192:195], v[30:31], off offset:-4096 nt
	global_load_dwordx4 v[196:199], v[76:77], off nt
	global_load_dwordx4 v[200:203], v[78:79], off nt
	global_load_dwordx4 v[204:207], v[76:77], off offset:-4096 nt
	s_add_u32 s14, s14, 0x8000
	s_addc_u32 s15, s15, 0
	s_add_u32 s26, s26, 0x14000
	s_addc_u32 s27, s27, 0
	s_add_i32 s41, s41, -4
	v_add_co_u32_e32 v2, vcc, s40, v2
	s_cmp_eq_u32 s41, 0
	s_nop 0
	v_addc_co_u32_e32 v3, vcc, 0, v3, vcc
	s_waitcnt vmcnt(9)
	v_mov_b32_e32 v38, v160
	v_mov_b32_e32 v39, v161
	v_mov_b32_e32 v40, v162
	v_mov_b32_e32 v41, v163
	v_mov_b32_e32 v54, v164
	v_mov_b32_e32 v55, v165
	v_mov_b32_e32 v56, v166
	v_mov_b32_e32 v57, v167
	v_mov_b32_e32 v50, v168
	v_mov_b32_e32 v51, v169
	v_mov_b32_e32 v52, v170
	v_mov_b32_e32 v53, v171
	v_lshlrev_b32_e32 v48, 16, v38
	v_lshlrev_b32_e32 v86, 16, v54
	v_and_b32_e32 v87, 0xffff0000, v54
	v_lshlrev_b32_e32 v82, 16, v50
	v_and_b32_e32 v83, 0xffff0000, v50
	v_lshlrev_b32_e32 v50, 16, v51
	v_and_b32_e32 v51, 0xffff0000, v51
	v_lshlrev_b32_e32 v84, 16, v52
	v_and_b32_e32 v85, 0xffff0000, v52
	v_lshlrev_b32_e32 v52, 16, v53
	v_and_b32_e32 v53, 0xffff0000, v53
	v_lshlrev_b32_e32 v54, 16, v55
	v_and_b32_e32 v55, 0xffff0000, v55
	v_lshlrev_b32_e32 v88, 16, v56
	v_and_b32_e32 v89, 0xffff0000, v56
	v_lshlrev_b32_e32 v56, 16, v57
	v_and_b32_e32 v57, 0xffff0000, v57
	v_pk_mul_f32 v[50:51], v[50:51], v[54:55]
	v_pk_mul_f32 v[54:55], v[82:83], v[86:87]
	v_pk_mul_f32 v[52:53], v[52:53], v[56:57]
	v_pk_mul_f32 v[56:57], v[84:85], v[88:89]
	v_and_b32_e32 v49, 0xffff0000, v38
	v_lshlrev_b32_e32 v38, 16, v39
	v_and_b32_e32 v39, 0xffff0000, v39
	v_lshlrev_b32_e32 v80, 16, v40
	v_and_b32_e32 v81, 0xffff0000, v40
	v_lshlrev_b32_e32 v40, 16, v41
	v_and_b32_e32 v41, 0xffff0000, v41
	v_pk_fma_f32 v[68:69], v[24:25], v[54:55], v[68:69]
	v_pk_fma_f32 v[66:67], v[26:27], v[50:51], v[66:67]
	v_pk_fma_f32 v[70:71], v[20:21], v[56:57], v[70:71]
	v_pk_fma_f32 v[42:43], v[22:23], v[52:53], v[42:43]
	v_pk_mul_f32 v[38:39], v[66:67], v[38:39]
	v_pk_mul_f32 v[48:49], v[68:69], v[48:49]
	v_pk_mul_f32 v[40:41], v[42:43], v[40:41]
	v_pk_mul_f32 v[42:43], v[70:71], v[80:81]
	v_pk_fma_f32 v[58:59], v[18:19], v[50:51], v[58:59]
	v_pk_mul_f32 v[82:83], v[10:11], v[50:51]
	v_bfe_u32 v1, v48, 16, 1
	v_bfe_u32 v50, v38, 16, 1
	v_bfe_u32 v66, v42, 16, 1
	v_bfe_u32 v68, v40, 16, 1
	v_bfe_u32 v45, v49, 16, 1
	v_bfe_u32 v51, v39, 16, 1
	v_bfe_u32 v67, v43, 16, 1
	v_bfe_u32 v69, v41, 16, 1
	v_add3_u32 v1, v48, v1, s28
	v_add3_u32 v38, v38, v50, s28
	v_add3_u32 v42, v42, v66, s28
	v_add3_u32 v40, v40, v68, s28
	v_add3_u32 v45, v49, v45, s28
	v_add3_u32 v39, v39, v51, s28
	v_add3_u32 v43, v43, v67, s28
	v_add3_u32 v41, v41, v69, s28
	v_lshrrev_b32_e32 v1, 16, v1
	v_lshrrev_b32_e32 v48, 16, v38
	v_lshrrev_b32_e32 v42, 16, v42
	v_lshrrev_b32_e32 v49, 16, v40
	v_and_or_b32 v38, v45, s25, v1
	v_and_or_b32 v39, v39, s25, v48
	v_and_or_b32 v40, v43, s25, v42
	v_and_or_b32 v41, v41, s25, v49
	global_store_dwordx4 v[36:37], v[38:41], off nt
	s_nop 0
	v_pk_fma_f32 v[60:61], v[16:17], v[54:55], v[60:61]
	v_pk_fma_f32 v[62:63], v[14:15], v[52:53], v[62:63]
	v_pk_fma_f32 v[64:65], v[12:13], v[56:57], v[64:65]
	v_pk_mul_f32 v[54:55], v[8:9], v[54:55]
	v_pk_mul_f32 v[56:57], v[4:5], v[56:57]
	v_pk_mul_f32 v[52:53], v[6:7], v[52:53]
	s_waitcnt vmcnt(7)
; #define GAS __attribute__((address_space(1)))
; __device__ __forceinline__ u32x2 pack4(f32x4 v) { u32x2 w; w.x = pk2(v.x, v.y); w.y = pk2(v.z, v.w); return w; }
; __device__ __forceinline__ f32x4 unpack4(u32x2 w) { return (f32x4){bflo(w.x), bfhi(w.x), bflo(w.y), bfhi(w.y)}; }
; __device__ __forceinline__ void phase4(KP kp, int wave, int bid, int G) {
;     ...
;         for (int i = 0; i < 16; ++i) { const int t = t0 + i; const bf16* r = R + (size_t)t * 10240 + ch;
;             const v4u b = *(const GAS v4u*)r, c = *(const GAS v4u*)(r + 2048), h = *(const GAS v4u*)(r + 4096);
;             const f32x4 ua = unpack4((u32x2){c.x, c.y}) * unpack4((u32x2){h.x, h.y}), ub = unpack4((u32x2){c.z, c.w}) * unpack4((u32x2){h.z, h.w});
;             const f32x4 ya = unpack4((u32x2){b.x, b.y}) * (w0a * u2a + w1a * u1a + w2a * ua), yb = unpack4((u32x2){b.z, b.w}) * (w0b * u2b + w1b * u1b + w2b * ub);
;             const u32x2 pa = pack4(ya), pb = pack4(yb);
;             *(GAS v4u*)(CV + (size_t)t * 4096 + ch) = (v4u){pa.x, pa.y, pb.x, pb.y};
;             u2a = u1a; u2b = u1b; u1a = ua; u1b = ub; }
	v_mov_b32_e32 v36, v172
	v_mov_b32_e32 v37, v173
	v_mov_b32_e32 v38, v174
	v_mov_b32_e32 v39, v175
	v_mov_b32_e32 v40, v176
	v_mov_b32_e32 v41, v177
	v_mov_b32_e32 v42, v178
	v_mov_b32_e32 v43, v179
	v_mov_b32_e32 v48, v180
	v_mov_b32_e32 v49, v181
	v_mov_b32_e32 v50, v182
	v_mov_b32_e32 v51, v183
	v_lshlrev_b32_e32 v34, 16, v36
	v_and_b32_e32 v35, 0xffff0000, v36
	v_lshlrev_b32_e32 v36, 16, v37
	v_and_b32_e32 v37, 0xffff0000, v37
	v_lshlrev_b32_e32 v66, 16, v40
	v_and_b32_e32 v67, 0xffff0000, v40
	v_lshlrev_b32_e32 v40, 16, v41
	v_and_b32_e32 v41, 0xffff0000, v41
	v_lshlrev_b32_e32 v68, 16, v38
	v_and_b32_e32 v69, 0xffff0000, v38
	v_lshlrev_b32_e32 v38, 16, v39
	v_and_b32_e32 v39, 0xffff0000, v39
	v_lshlrev_b32_e32 v70, 16, v42
	v_and_b32_e32 v71, 0xffff0000, v42
	v_lshlrev_b32_e32 v42, 16, v43
	v_and_b32_e32 v43, 0xffff0000, v43
	v_pk_mul_f32 v[84:85], v[36:37], v[40:41]
	v_pk_mul_f32 v[66:67], v[34:35], v[66:67]
	v_pk_mul_f32 v[86:87], v[38:39], v[42:43]
	v_pk_mul_f32 v[68:69], v[68:69], v[70:71]
	v_lshlrev_b32_e32 v72, 16, v48
	v_and_b32_e32 v73, 0xffff0000, v48
	v_lshlrev_b32_e32 v48, 16, v49
	v_and_b32_e32 v49, 0xffff0000, v49
	v_lshlrev_b32_e32 v80, 16, v50
	v_and_b32_e32 v81, 0xffff0000, v50
	v_lshlrev_b32_e32 v50, 16, v51
	v_and_b32_e32 v51, 0xffff0000, v51
	v_pk_fma_f32 v[34:35], v[24:25], v[66:67], v[60:61]
	v_pk_fma_f32 v[36:37], v[26:27], v[84:85], v[58:59]
	v_pk_fma_f32 v[38:39], v[20:21], v[68:69], v[64:65]
	v_pk_fma_f32 v[40:41], v[22:23], v[86:87], v[62:63]
	v_pk_mul_f32 v[36:37], v[36:37], v[48:49]
	v_pk_mul_f32 v[34:35], v[34:35], v[72:73]
	v_pk_mul_f32 v[40:41], v[40:41], v[50:51]
	v_pk_mul_f32 v[38:39], v[38:39], v[80:81]
	v_bfe_u32 v1, v34, 16, 1
	v_bfe_u32 v45, v35, 16, 1
	v_bfe_u32 v48, v36, 16, 1
	v_bfe_u32 v49, v37, 16, 1
	v_bfe_u32 v50, v38, 16, 1
	v_bfe_u32 v51, v39, 16, 1
	v_bfe_u32 v58, v40, 16, 1
	v_bfe_u32 v59, v41, 16, 1
	v_add3_u32 v1, v34, v1, s28
	v_add3_u32 v34, v35, v45, s28
	v_add3_u32 v35, v36, v48, s28
	v_add3_u32 v36, v37, v49, s28
	v_add3_u32 v37, v38, v50, s28
	v_add3_u32 v38, v39, v51, s28
	v_add3_u32 v39, v40, v58, s28
	v_add3_u32 v40, v41, v59, s28
	v_lshrrev_b32_e32 v1, 16, v1
	v_lshrrev_b32_e32 v35, 16, v35
	v_lshrrev_b32_e32 v37, 16, v37
	v_lshrrev_b32_e32 v39, 16, v39
	v_and_or_b32 v34, v34, s25, v1
	v_and_or_b32 v35, v36, s25, v35
	v_and_or_b32 v36, v38, s25, v37
	v_and_or_b32 v37, v40, s25, v39
	global_store_dwordx4 v[28:29], v[34:37], off nt
	s_nop 0
	s_nop 0
	v_pk_fma_f32 v[42:43], v[18:19], v[84:85], v[82:83]
	v_pk_fma_f32 v[54:55], v[16:17], v[66:67], v[54:55]
	v_pk_fma_f32 v[52:53], v[14:15], v[86:87], v[52:53]
	v_pk_fma_f32 v[56:57], v[12:13], v[68:69], v[56:57]
	s_waitcnt vmcnt(5)
; #define GAS __attribute__((address_space(1)))
; __device__ __forceinline__ u32x2 pack4(f32x4 v) { u32x2 w; w.x = pk2(v.x, v.y); w.y = pk2(v.z, v.w); return w; }
; __device__ __forceinline__ f32x4 unpack4(u32x2 w) { return (f32x4){bflo(w.x), bfhi(w.x), bflo(w.y), bfhi(w.y)}; }
; __device__ __forceinline__ void phase4(KP kp, int wave, int bid, int G) {
;     ...
;         for (int i = 0; i < 16; ++i) { const int t = t0 + i; const bf16* r = R + (size_t)t * 10240 + ch;
;             const v4u b = *(const GAS v4u*)r, c = *(const GAS v4u*)(r + 2048), h = *(const GAS v4u*)(r + 4096);
;             const f32x4 ua = unpack4((u32x2){c.x, c.y}) * unpack4((u32x2){h.x, h.y}), ub = unpack4((u32x2){c.z, c.w}) * unpack4((u32x2){h.z, h.w});
;             const f32x4 ya = unpack4((u32x2){b.x, b.y}) * (w0a * u2a + w1a * u1a + w2a * ua), yb = unpack4((u32x2){b.z, b.w}) * (w0b * u2b + w1b * u1b + w2b * ub);
;             const u32x2 pa = pack4(ya), pb = pack4(yb);
;             *(GAS v4u*)(CV + (size_t)t * 4096 + ch) = (v4u){pa.x, pa.y, pb.x, pb.y};
;             u2a = u1a; u2b = u1b; u1a = ua; u1b = ub; }
	v_mov_b32_e32 v34, v184
	v_mov_b32_e32 v35, v185
	v_mov_b32_e32 v36, v186
	v_mov_b32_e32 v37, v187
	v_mov_b32_e32 v38, v188
	v_mov_b32_e32 v39, v189
	v_mov_b32_e32 v40, v190
	v_mov_b32_e32 v41, v191
	v_mov_b32_e32 v28, v192
	v_mov_b32_e32 v29, v193
	v_mov_b32_e32 v30, v194
	v_mov_b32_e32 v31, v195
	v_lshlrev_b32_e32 v32, 16, v34
	v_and_b32_e32 v33, 0xffff0000, v34
	v_lshlrev_b32_e32 v34, 16, v35
	v_and_b32_e32 v35, 0xffff0000, v35
	v_lshlrev_b32_e32 v48, 16, v38
	v_and_b32_e32 v49, 0xffff0000, v38
	v_lshlrev_b32_e32 v38, 16, v39
	v_and_b32_e32 v39, 0xffff0000, v39
	v_lshlrev_b32_e32 v50, 16, v36
	v_and_b32_e32 v51, 0xffff0000, v36
	v_lshlrev_b32_e32 v36, 16, v37
	v_and_b32_e32 v37, 0xffff0000, v37
	v_lshlrev_b32_e32 v58, 16, v40
	v_and_b32_e32 v59, 0xffff0000, v40
	v_lshlrev_b32_e32 v40, 16, v41
	v_and_b32_e32 v41, 0xffff0000, v41
	v_lshlrev_b32_e32 v60, 16, v28
	v_and_b32_e32 v61, 0xffff0000, v28
	v_lshlrev_b32_e32 v62, 16, v29
	v_and_b32_e32 v63, 0xffff0000, v29
	v_lshlrev_b32_e32 v64, 16, v30
	v_and_b32_e32 v65, 0xffff0000, v30
	v_lshlrev_b32_e32 v70, 16, v31
	v_and_b32_e32 v71, 0xffff0000, v31
	v_pk_mul_f32 v[34:35], v[34:35], v[38:39]
	v_pk_mul_f32 v[32:33], v[32:33], v[48:49]
	v_pk_mul_f32 v[30:31], v[36:37], v[40:41]
	v_pk_mul_f32 v[28:29], v[50:51], v[58:59]
	v_pk_fma_f32 v[36:37], v[24:25], v[32:33], v[54:55]
	v_pk_fma_f32 v[38:39], v[26:27], v[34:35], v[42:43]
	v_pk_fma_f32 v[40:41], v[20:21], v[28:29], v[56:57]
	v_pk_fma_f32 v[42:43], v[22:23], v[30:31], v[52:53]
	v_pk_mul_f32 v[38:39], v[38:39], v[62:63]
	v_pk_mul_f32 v[36:37], v[36:37], v[60:61]
	v_pk_mul_f32 v[42:43], v[42:43], v[70:71]
	v_pk_mul_f32 v[40:41], v[40:41], v[64:65]
	v_bfe_u32 v1, v36, 16, 1
	v_bfe_u32 v45, v37, 16, 1
	v_bfe_u32 v48, v38, 16, 1
	v_bfe_u32 v49, v39, 16, 1
	v_bfe_u32 v50, v40, 16, 1
	v_bfe_u32 v51, v41, 16, 1
	v_bfe_u32 v52, v42, 16, 1
	v_bfe_u32 v53, v43, 16, 1
	v_add3_u32 v1, v36, v1, s28
	v_add3_u32 v36, v37, v45, s28
	v_add3_u32 v37, v38, v48, s28
	v_add3_u32 v38, v39, v49, s28
	v_add3_u32 v39, v40, v50, s28
	v_add3_u32 v40, v41, v51, s28
	v_add3_u32 v41, v42, v52, s28
	v_add3_u32 v42, v43, v53, s28
	v_lshrrev_b32_e32 v1, 16, v1
	v_lshrrev_b32_e32 v37, 16, v37
	v_lshrrev_b32_e32 v39, 16, v39
	v_lshrrev_b32_e32 v41, 16, v41
	v_and_or_b32 v36, v36, s25, v1
	v_and_or_b32 v37, v38, s25, v37
	v_and_or_b32 v38, v40, s25, v39
	v_and_or_b32 v39, v42, s25, v41
	global_store_dwordx4 v[74:75], v[36:39], off nt
	s_nop 0
	v_pk_mul_f32 v[52:53], v[8:9], v[66:67]
	v_pk_mul_f32 v[54:55], v[10:11], v[84:85]
	v_pk_mul_f32 v[56:57], v[4:5], v[68:69]
	v_pk_mul_f32 v[58:59], v[6:7], v[86:87]
	v_pk_fma_f32 v[54:55], v[18:19], v[34:35], v[54:55]
	v_pk_fma_f32 v[52:53], v[16:17], v[32:33], v[52:53]
	v_pk_fma_f32 v[58:59], v[14:15], v[30:31], v[58:59]
	v_pk_fma_f32 v[56:57], v[12:13], v[28:29], v[56:57]
	s_waitcnt vmcnt(3)
	v_mov_b32_e32 v36, v196
	v_mov_b32_e32 v37, v197
	v_mov_b32_e32 v38, v198
	v_mov_b32_e32 v39, v199
	v_mov_b32_e32 v40, v200
	v_mov_b32_e32 v41, v201
	v_mov_b32_e32 v42, v202
	v_mov_b32_e32 v43, v203
	v_mov_b32_e32 v48, v204
	v_mov_b32_e32 v49, v205
	v_mov_b32_e32 v50, v206
	v_mov_b32_e32 v51, v207
	v_lshlrev_b32_e32 v60, 16, v36
	v_and_b32_e32 v61, 0xffff0000, v36
	v_lshlrev_b32_e32 v36, 16, v37
	v_and_b32_e32 v37, 0xffff0000, v37
	v_lshlrev_b32_e32 v62, 16, v40
	v_and_b32_e32 v63, 0xffff0000, v40
	v_lshlrev_b32_e32 v40, 16, v41
	v_and_b32_e32 v41, 0xffff0000, v41
	v_lshlrev_b32_e32 v64, 16, v38
	v_and_b32_e32 v65, 0xffff0000, v38
	v_lshlrev_b32_e32 v66, 16, v39
	v_and_b32_e32 v67, 0xffff0000, v39
	v_lshlrev_b32_e32 v68, 16, v42
	v_and_b32_e32 v69, 0xffff0000, v42
	v_lshlrev_b32_e32 v42, 16, v43
	v_and_b32_e32 v43, 0xffff0000, v43
	v_pk_mul_f32 v[38:39], v[36:37], v[40:41]
	v_pk_mul_f32 v[36:37], v[60:61], v[62:63]
	v_pk_mul_f32 v[42:43], v[66:67], v[42:43]
	v_pk_mul_f32 v[40:41], v[64:65], v[68:69]
	v_lshlrev_b32_e32 v70, 16, v48
	v_and_b32_e32 v71, 0xffff0000, v48
	v_lshlrev_b32_e32 v48, 16, v49
	v_and_b32_e32 v49, 0xffff0000, v49
	v_lshlrev_b32_e32 v72, 16, v50
	v_and_b32_e32 v73, 0xffff0000, v50
	v_lshlrev_b32_e32 v50, 16, v51
	v_and_b32_e32 v51, 0xffff0000, v51
	v_pk_fma_f32 v[52:53], v[24:25], v[36:37], v[52:53]
	v_pk_fma_f32 v[54:55], v[26:27], v[38:39], v[54:55]
	v_pk_fma_f32 v[56:57], v[20:21], v[40:41], v[56:57]
	v_pk_fma_f32 v[58:59], v[22:23], v[42:43], v[58:59]
	v_pk_mul_f32 v[48:49], v[54:55], v[48:49]
	v_pk_mul_f32 v[52:53], v[52:53], v[70:71]
	v_pk_mul_f32 v[50:51], v[58:59], v[50:51]
	v_pk_mul_f32 v[54:55], v[56:57], v[72:73]
	v_bfe_u32 v1, v52, 16, 1
	v_bfe_u32 v56, v48, 16, 1
	v_bfe_u32 v58, v54, 16, 1
	v_bfe_u32 v60, v50, 16, 1
	v_bfe_u32 v45, v53, 16, 1
	v_bfe_u32 v57, v49, 16, 1
	v_bfe_u32 v59, v55, 16, 1
	v_bfe_u32 v61, v51, 16, 1
	v_add3_u32 v1, v52, v1, s28
	v_add3_u32 v48, v48, v56, s28
	v_add3_u32 v52, v54, v58, s28
	v_add3_u32 v50, v50, v60, s28
	v_add3_u32 v45, v53, v45, s28
	v_add3_u32 v49, v49, v57, s28
	v_add3_u32 v53, v55, v59, s28
	v_add3_u32 v51, v51, v61, s28
	v_lshrrev_b32_e32 v1, 16, v1
	v_lshrrev_b32_e32 v54, 16, v48
	v_lshrrev_b32_e32 v52, 16, v52
	v_lshrrev_b32_e32 v55, 16, v50
	v_and_or_b32 v48, v45, s25, v1
	v_and_or_b32 v49, v49, s25, v54
	v_and_or_b32 v50, v53, s25, v52
	v_and_or_b32 v51, v51, s25, v55
	global_store_dwordx4 v[2:3], v[48:51], off nt
	s_cbranch_scc0 .LBB0_715
	s_add_i32 s17, s17, s18
	s_add_i32 s20, s20, s21
	s_add_i32 s22, s22, s23
	s_cmpk_gt_i32 s17, 0x7ff
	s_cbranch_scc0 .LBB0_712

; #define GAS __attribute__((address_space(1)))
; #define LAS __attribute__((address_space(3)))
; __device__ __forceinline__ u32x2 pack4(f32x4 v) { u32x2 w; w.x = pk2(v.x, v.y); w.y = pk2(v.z, v.w); return w; }
; __device__ __forceinline__ void phase8(KP kp, LAS unsigned char* lds, int wave, int bid) {
;     ...
;         GAS u32x2* o8 = (GAS u32x2*)(H + (size_t)t * DM) + lane;
; #pragma unroll
;         for (int j = 0; j < 8; ++j) { const f32x4 av = *(const LAS f32x4*)(A2 + 256 * j + 4 * lane), bv = *(const LAS f32x4*)(B2 + 256 * j + 4 * lane);
;             o8[64 * j] = pack4(v[j] * rstd * av + bv); }
.LBB0_932:
	s_or_b64 exec, exec, s[6:7]
	ds_read_b128 v[52:55], v50
	ds_read_b128 v[56:59], v50 offset:8192
	v_pk_mul_f32 v[66:67], v[28:29], v[42:43] op_sel_hi:[1,0]
	v_pk_mul_f32 v[64:65], v[30:31], v[42:43] op_sel_hi:[1,0]
	ds_read_b128 v[28:31], v50 offset:1024
	ds_read_b128 v[60:63], v50 offset:9216
	v_add_co_u32_e32 v40, vcc, s29, v40
	s_waitcnt lgkmcnt(2)
	v_pk_fma_f32 v[52:53], v[66:67], v[52:53], v[56:57]
	v_pk_fma_f32 v[54:55], v[64:65], v[54:55], v[58:59]
	v_bfe_u32 v43, v52, 16, 1
	v_add3_u32 v43, v52, v43, s22
	v_bfe_u32 v44, v53, 16, 1
	v_lshrrev_b32_e32 v43, 16, v43
	v_add3_u32 v44, v53, v44, s22
	v_and_or_b32 v52, v44, s23, v43
	v_bfe_u32 v43, v54, 16, 1
	v_add3_u32 v43, v54, v43, s22
	v_lshrrev_b32_e32 v43, 16, v43
	v_pk_mul_f32 v[24:25], v[24:25], v[42:43] op_sel_hi:[1,0]
	v_pk_mul_f32 v[26:27], v[26:27], v[42:43] op_sel_hi:[1,0]
	s_waitcnt lgkmcnt(0)
	v_pk_fma_f32 v[24:25], v[24:25], v[28:29], v[60:61]
	v_pk_fma_f32 v[26:27], v[26:27], v[30:31], v[62:63]
	v_bfe_u32 v28, v24, 16, 1
	v_add3_u32 v24, v24, v28, s22
	v_bfe_u32 v28, v25, 16, 1
	v_lshrrev_b32_e32 v24, 16, v24
	v_add3_u32 v25, v25, v28, s22
	v_and_or_b32 v24, v25, s23, v24
	v_bfe_u32 v25, v26, 16, 1
	v_bfe_u32 v44, v55, 16, 1
	v_add3_u32 v25, v26, v25, s22
	v_bfe_u32 v26, v27, 16, 1
	v_add3_u32 v44, v55, v44, s22
	v_lshrrev_b32_e32 v25, 16, v25
	v_add3_u32 v26, v27, v26, s22
	v_and_or_b32 v53, v44, s23, v43
	v_addc_co_u32_e32 v41, vcc, 0, v41, vcc
	v_and_or_b32 v25, v26, s23, v25
	global_store_dwordx2 v[40:41], v[52:53], off nt
	global_store_dwordx2 v[40:41], v[24:25], off offset:512 nt
	ds_read_b128 v[24:27], v50 offset:2048
	ds_read_b128 v[28:31], v50 offset:10240
	v_pk_mul_f32 v[56:57], v[22:23], v[42:43] op_sel_hi:[1,0]
	v_pk_mul_f32 v[58:59], v[20:21], v[42:43] op_sel_hi:[1,0]
	ds_read_b128 v[20:23], v50 offset:3072
	ds_read_b128 v[52:55], v50 offset:11264
	v_pk_mul_f32 v[16:17], v[16:17], v[42:43] op_sel_hi:[1,0]
	s_waitcnt lgkmcnt(2)
	v_pk_fma_f32 v[24:25], v[58:59], v[24:25], v[28:29]
	v_pk_mul_f32 v[18:19], v[18:19], v[42:43] op_sel_hi:[1,0]
	v_bfe_u32 v28, v24, 16, 1
	s_waitcnt lgkmcnt(0)
	v_pk_fma_f32 v[16:17], v[16:17], v[20:21], v[52:53]
	v_add3_u32 v24, v24, v28, s22
	v_bfe_u32 v20, v16, 16, 1
	v_bfe_u32 v28, v25, 16, 1
	v_add3_u32 v16, v16, v20, s22
	v_bfe_u32 v20, v17, 16, 1
	v_pk_fma_f32 v[26:27], v[56:57], v[26:27], v[30:31]
	v_lshrrev_b32_e32 v24, 16, v24
	v_add3_u32 v25, v25, v28, s22
	v_pk_fma_f32 v[18:19], v[18:19], v[22:23], v[54:55]
	v_lshrrev_b32_e32 v16, 16, v16
	v_add3_u32 v17, v17, v20, s22
	v_and_or_b32 v24, v25, s23, v24
	v_bfe_u32 v25, v26, 16, 1
	v_and_or_b32 v16, v17, s23, v16
	v_bfe_u32 v17, v18, 16, 1
	v_add3_u32 v25, v26, v25, s22
	v_bfe_u32 v26, v27, 16, 1
	v_add3_u32 v17, v18, v17, s22
	v_bfe_u32 v18, v19, 16, 1
	v_lshrrev_b32_e32 v25, 16, v25
	v_add3_u32 v26, v27, v26, s22
	v_lshrrev_b32_e32 v17, 16, v17
	v_add3_u32 v18, v19, v18, s22
	v_and_or_b32 v25, v26, s23, v25
	v_and_or_b32 v17, v18, s23, v17
	global_store_dwordx2 v[40:41], v[24:25], off offset:1024 nt
	global_store_dwordx2 v[40:41], v[16:17], off offset:1536 nt
	ds_read_b128 v[16:19], v50 offset:4096
	ds_read_b128 v[20:23], v50 offset:12288
	v_pk_mul_f32 v[28:29], v[14:15], v[42:43] op_sel_hi:[1,0]
	v_pk_mul_f32 v[30:31], v[12:13], v[42:43] op_sel_hi:[1,0]
	ds_read_b128 v[12:15], v50 offset:5120
	ds_read_b128 v[24:27], v50 offset:13312
	v_pk_mul_f32 v[8:9], v[8:9], v[42:43] op_sel_hi:[1,0]
	s_waitcnt lgkmcnt(2)
	v_pk_fma_f32 v[16:17], v[30:31], v[16:17], v[20:21]
	v_pk_mul_f32 v[10:11], v[10:11], v[42:43] op_sel_hi:[1,0]
	v_bfe_u32 v20, v16, 16, 1
	s_waitcnt lgkmcnt(0)
	v_pk_fma_f32 v[8:9], v[8:9], v[12:13], v[24:25]
	v_add3_u32 v16, v16, v20, s22
	v_bfe_u32 v12, v8, 16, 1
	v_bfe_u32 v20, v17, 16, 1
	v_add3_u32 v8, v8, v12, s22
	v_bfe_u32 v12, v9, 16, 1
	v_pk_fma_f32 v[18:19], v[28:29], v[18:19], v[22:23]
	v_lshrrev_b32_e32 v16, 16, v16
	v_add3_u32 v17, v17, v20, s22
	v_pk_fma_f32 v[10:11], v[10:11], v[14:15], v[26:27]
	v_lshrrev_b32_e32 v8, 16, v8
	v_add3_u32 v9, v9, v12, s22
	v_and_or_b32 v16, v17, s23, v16
	v_bfe_u32 v17, v18, 16, 1
	v_and_or_b32 v8, v9, s23, v8
	v_bfe_u32 v9, v10, 16, 1
	v_add3_u32 v17, v18, v17, s22
	v_bfe_u32 v18, v19, 16, 1
	v_add3_u32 v9, v10, v9, s22
	v_bfe_u32 v10, v11, 16, 1
	v_lshrrev_b32_e32 v17, 16, v17
	v_add3_u32 v18, v19, v18, s22
	v_lshrrev_b32_e32 v9, 16, v9
	v_add3_u32 v10, v11, v10, s22
	v_and_or_b32 v17, v18, s23, v17
	v_and_or_b32 v9, v10, s23, v9
	global_store_dwordx2 v[40:41], v[16:17], off offset:2048 nt
	global_store_dwordx2 v[40:41], v[8:9], off offset:2560 nt
	ds_read_b128 v[8:11], v50 offset:6144
	ds_read_b128 v[12:15], v50 offset:14336
	v_pk_mul_f32 v[20:21], v[6:7], v[42:43] op_sel_hi:[1,0]
	v_pk_mul_f32 v[22:23], v[4:5], v[42:43] op_sel_hi:[1,0]
	ds_read_b128 v[4:7], v50 offset:7168
	ds_read_b128 v[16:19], v50 offset:15360
	v_pk_mul_f32 v[0:1], v[0:1], v[42:43] op_sel_hi:[1,0]
	s_waitcnt lgkmcnt(2)
	v_pk_fma_f32 v[8:9], v[22:23], v[8:9], v[12:13]
	v_pk_mul_f32 v[2:3], v[2:3], v[42:43] op_sel_hi:[1,0]
	v_bfe_u32 v12, v8, 16, 1
	s_waitcnt lgkmcnt(0)
	v_pk_fma_f32 v[0:1], v[0:1], v[4:5], v[16:17]
	v_add3_u32 v8, v8, v12, s22
	v_bfe_u32 v4, v0, 16, 1
	v_bfe_u32 v12, v9, 16, 1
	v_add3_u32 v0, v0, v4, s22
	v_bfe_u32 v4, v1, 16, 1
	v_pk_fma_f32 v[10:11], v[20:21], v[10:11], v[14:15]
	v_lshrrev_b32_e32 v8, 16, v8
	v_add3_u32 v9, v9, v12, s22
	v_pk_fma_f32 v[2:3], v[2:3], v[6:7], v[18:19]
	v_lshrrev_b32_e32 v0, 16, v0
	v_add3_u32 v1, v1, v4, s22
	v_and_or_b32 v8, v9, s23, v8
	v_bfe_u32 v9, v10, 16, 1
	v_and_or_b32 v0, v1, s23, v0
	v_bfe_u32 v1, v2, 16, 1
	v_add3_u32 v9, v10, v9, s22
	v_bfe_u32 v10, v11, 16, 1
	v_add3_u32 v1, v2, v1, s22
	v_bfe_u32 v2, v3, 16, 1
	v_lshrrev_b32_e32 v9, 16, v9
	v_add3_u32 v10, v11, v10, s22
	v_lshrrev_b32_e32 v1, 16, v1
	v_add3_u32 v2, v3, v2, s22
	s_add_i32 s18, s18, 8
	v_and_or_b32 v9, v10, s23, v9
	v_and_or_b32 v1, v2, s23, v1
	v_lshl_add_u64 v[36:37], v[36:37], 0, s[14:15]
	s_cmp_eq_u32 s18, 16
	v_lshl_add_u64 v[38:39], v[38:39], 0, s[26:27]
	global_store_dwordx2 v[40:41], v[8:9], off offset:3072 nt
	global_store_dwordx2 v[40:41], v[0:1], off offset:3584 nt
	s_cbranch_scc1 .LBB0_937
; #define GAS __attribute__((address_space(1)))
; #define LAS __attribute__((address_space(3)))
; __device__ __forceinline__ float dot4(f32x4 a, f32x4 b) { return (a.x * b.x + a.y * b.y) + (a.z * b.z + a.w * b.w); }
; __device__ __forceinline__ u32x2 pack4(f32x4 v) { u32x2 w; w.x = pk2(v.x, v.y); w.y = pk2(v.z, v.w); return w; }
; __device__ __forceinline__ void phase8(KP kp, LAS unsigned char* lds, int wave, int bid) {
;     ...
;     for (int q = 0; q < 4; ++q) {
;         const int lt = 4 * wave + q, t = 32 * bid + lt;
;         const GAS f32x4* xr = (const GAS f32x4*)(X1 + (size_t)t * DM) + lane;
;         f32x4 v[8]; float s = 0.f;
; #pragma unroll
;         for (int j = 0; j < 8; ++j) { v[j] = xr[64 * j]; s += dot4(v[j], v[j]); }
;         const float rstd = 1.0f / sqrtf(wave_sum(s) * (1.0f / DM) + EPS);
;         if (lane == 0) rs[lt] = rstd;
;         GAS u32x2* o8 = (GAS u32x2*)(H + (size_t)t * DM) + lane;
; #pragma unroll
;         for (int j = 0; j < 8; ++j) { const f32x4 av = *(const LAS f32x4*)(A2 + 256 * j + 4 * lane), bv = *(const LAS f32x4*)(B2 + 256 * j + 4 * lane);
;             o8[64 * j] = pack4(v[j] * rstd * av + bv); }
.LBB0_933:
	v_lshl_add_u64 v[42:43], s[8:9], 0, v[38:39]
	v_add_co_u32_e32 v16, vcc, s20, v42
	s_nop 1
	v_addc_co_u32_e32 v17, vcc, 0, v43, vcc
	global_load_dwordx4 v[12:15], v[16:17], off
	v_add_co_u32_e32 v40, vcc, 0x56000000, v42
	global_load_dwordx4 v[8:11], v[16:17], off offset:1024
	global_load_dwordx4 v[4:7], v[16:17], off offset:2048
	global_load_dwordx4 v[0:3], v[16:17], off offset:3072
	v_addc_co_u32_e32 v41, vcc, 0, v43, vcc
	global_load_dwordx4 v[28:31], v[40:41], off
	global_load_dwordx4 v[24:27], v[40:41], off offset:1024
	global_load_dwordx4 v[20:23], v[40:41], off offset:2048
	global_load_dwordx4 v[16:19], v[40:41], off offset:3072
	v_add_co_u32_e32 v192, vcc, s28, v42
	s_nop 1
	v_addc_co_u32_e32 v193, vcc, 0, v43, vcc
	v_add_co_u32_e32 v194, vcc, s25, v42
	s_nop 1
	v_addc_co_u32_e32 v195, vcc, 0, v43, vcc
	global_load_dwordx4 v[188:191], v[192:193], off offset:-4096
	global_load_dwordx4 v[184:187], v[194:195], off offset:1024
	global_load_dwordx4 v[180:183], v[194:195], off offset:2048
	global_load_dwordx4 v[176:179], v[194:195], off offset:3072
	global_load_dwordx4 v[172:175], v[192:193], off
	global_load_dwordx4 v[168:171], v[192:193], off offset:1024
	global_load_dwordx4 v[164:167], v[192:193], off offset:2048
	global_load_dwordx4 v[160:163], v[192:193], off offset:3072
	s_waitcnt vmcnt(15)
	v_mul_f32_e32 v40, v13, v13
	v_mul_f32_e32 v41, v15, v15
	s_waitcnt vmcnt(14)
	v_mul_f32_e32 v44, v9, v9
	v_mul_f32_e32 v52, v11, v11
	s_waitcnt vmcnt(13)
	v_mul_f32_e32 v53, v5, v5
	v_mul_f32_e32 v54, v7, v7
	s_waitcnt vmcnt(11)
	v_mul_f32_e32 v57, v29, v29
	v_mul_f32_e32 v58, v31, v31
	s_waitcnt vmcnt(10)
	v_mul_f32_e32 v59, v25, v25
	v_mul_f32_e32 v60, v27, v27
	v_mul_f32_e32 v55, v1, v1
	v_mul_f32_e32 v56, v3, v3
	s_waitcnt vmcnt(9)
	v_mul_f32_e32 v61, v21, v21
	v_mul_f32_e32 v62, v23, v23
	v_fmac_f32_e32 v40, v12, v12
	v_fmac_f32_e32 v41, v14, v14
	v_fmac_f32_e32 v44, v8, v8
	v_fmac_f32_e32 v52, v10, v10
	v_fmac_f32_e32 v53, v4, v4
	v_fmac_f32_e32 v54, v6, v6
	v_fmac_f32_e32 v57, v28, v28
	v_fmac_f32_e32 v58, v30, v30
	v_fmac_f32_e32 v59, v24, v24
	v_fmac_f32_e32 v60, v26, v26
	s_waitcnt vmcnt(8)
	v_mul_f32_e32 v63, v17, v17
	v_mul_f32_e32 v64, v19, v19
	v_fmac_f32_e32 v55, v0, v0
	v_fmac_f32_e32 v56, v2, v2
	v_fmac_f32_e32 v61, v20, v20
	v_fmac_f32_e32 v62, v22, v22
	v_add_f32_e32 v40, v40, v41
	v_add_f32_e32 v41, v44, v52
	v_add_f32_e32 v44, v53, v54
	v_add_f32_e32 v53, v57, v58
	v_add_f32_e32 v54, v59, v60
	v_fmac_f32_e32 v63, v16, v16
	v_fmac_f32_e32 v64, v18, v18
	v_add_f32_e32 v52, v55, v56
	v_add_f32_e32 v55, v61, v62
	v_add_f32_e32 v53, v53, v54
	v_add_f32_e32 v56, v63, v64
	v_add_f32_e32 v53, v53, v55
	v_add_f32_e32 v53, v53, v56
	v_add_f32_e32 v40, v53, v40
	v_add_f32_e32 v40, v40, v41
	v_add_f32_e32 v40, v40, v44
	v_add_f32_e32 v40, v40, v52
	s_nop 1
	v_add_f32_dpp v40, v40, v40 quad_perm:[1,0,3,2] row_mask:0xf bank_mask:0xf
	s_nop 1
	v_add_f32_dpp v40, v40, v40 quad_perm:[2,3,0,1] row_mask:0xf bank_mask:0xf
	s_nop 1
	v_add_f32_dpp v40, v40, v40 row_half_mirror row_mask:0xf bank_mask:0xf
	s_nop 1
	v_add_f32_dpp v40, v40, v40 row_mirror row_mask:0xf bank_mask:0xf
	v_mov_b32_e32 v41, v40
	s_nop 1
	v_permlane16_swap_b32_e32 v40, v41
	v_add_f32_e32 v40, v40, v41
	v_mov_b32_e32 v41, v40
	s_nop 1
	v_permlane32_swap_b32_e32 v40, v41
	v_add_f32_e32 v40, v40, v41
	v_fmamk_f32 v40, v40, 0x3a000000, v35
	v_mul_f32_e32 v41, 0x4f800000, v40
	v_cmp_gt_f32_e32 vcc, s21, v40
	s_nop 1
	v_cndmask_b32_e32 v40, v40, v41, vcc
	v_sqrt_f32_e32 v41, v40
	s_nop 0
	v_add_u32_e32 v44, -1, v41
	v_add_u32_e32 v52, 1, v41
	v_fma_f32 v53, -v44, v41, v40
	v_fma_f32 v54, -v52, v41, v40
	v_cmp_ge_f32_e64 s[6:7], 0, v53
	s_nop 1
	v_cndmask_b32_e64 v41, v41, v44, s[6:7]
	v_cmp_lt_f32_e64 s[6:7], 0, v54
	s_nop 1
	v_cndmask_b32_e64 v41, v41, v52, s[6:7]
	v_mul_f32_e32 v44, 0x37800000, v41
	v_cndmask_b32_e32 v41, v41, v44, vcc
	v_cmp_class_f32_e32 vcc, v40, v51
	s_nop 1
	v_cndmask_b32_e32 v40, v41, v40, vcc
	v_div_scale_f32 v41, s[6:7], v40, v40, 1.0
	v_rcp_f32_e32 v44, v41
	v_div_scale_f32 v52, vcc, 1.0, v40, 1.0
	v_fma_f32 v53, -v41, v44, 1.0
	v_fmac_f32_e32 v44, v53, v44
	v_mul_f32_e32 v53, v52, v44
	v_fma_f32 v54, -v41, v53, v52
	v_fmac_f32_e32 v53, v54, v44
	v_fma_f32 v41, -v41, v53, v52
	v_div_fmas_f32 v41, v41, v44, v53
	v_div_fixup_f32 v44, v41, v40, 1.0
	s_and_saveexec_b64 s[6:7], s[2:3]
	s_add_i32 s4, s5, s18
	v_mov_b32_e32 v40, s4
	ds_write_b32 v40, v44
	s_or_b64 exec, exec, s[6:7]
	ds_read_b128 v[52:55], v50
	ds_read_b128 v[56:59], v50 offset:8192
	v_pk_mul_f32 v[64:65], v[30:31], v[44:45] op_sel_hi:[1,0]
	v_pk_mul_f32 v[66:67], v[28:29], v[44:45] op_sel_hi:[1,0]
	ds_read_b128 v[28:31], v50 offset:1024
	ds_read_b128 v[60:63], v50 offset:9216
	v_pk_mul_f32 v[24:25], v[24:25], v[44:45] op_sel_hi:[1,0]
	s_waitcnt lgkmcnt(2)
	v_pk_fma_f32 v[52:53], v[66:67], v[52:53], v[56:57]
	v_pk_mul_f32 v[26:27], v[26:27], v[44:45] op_sel_hi:[1,0]
	v_bfe_u32 v56, v52, 16, 1
	s_waitcnt lgkmcnt(0)
; #define GAS __attribute__((address_space(1)))
; #define LAS __attribute__((address_space(3)))
; __device__ __forceinline__ u32x2 pack4(f32x4 v) { u32x2 w; w.x = pk2(v.x, v.y); w.y = pk2(v.z, v.w); return w; }
; __device__ __forceinline__ void phase8(KP kp, LAS unsigned char* lds, int wave, int bid) {
;     ...
;         GAS u32x2* o8 = (GAS u32x2*)(H + (size_t)t * DM) + lane;
; #pragma unroll
;         for (int j = 0; j < 8; ++j) { const f32x4 av = *(const LAS f32x4*)(A2 + 256 * j + 4 * lane), bv = *(const LAS f32x4*)(B2 + 256 * j + 4 * lane);
;             o8[64 * j] = pack4(v[j] * rstd * av + bv); }
	v_pk_fma_f32 v[24:25], v[24:25], v[28:29], v[60:61]
	v_add3_u32 v52, v52, v56, s22
	v_bfe_u32 v28, v24, 16, 1
	v_bfe_u32 v56, v53, 16, 1
	v_add3_u32 v24, v24, v28, s22
	v_bfe_u32 v28, v25, 16, 1
	v_pk_fma_f32 v[54:55], v[64:65], v[54:55], v[58:59]
	v_lshrrev_b32_e32 v52, 16, v52
	v_add3_u32 v53, v53, v56, s22
	v_pk_fma_f32 v[26:27], v[26:27], v[30:31], v[62:63]
	v_lshrrev_b32_e32 v24, 16, v24
	v_add3_u32 v25, v25, v28, s22
	v_and_or_b32 v52, v53, s23, v52
	v_bfe_u32 v53, v54, 16, 1
	v_and_or_b32 v24, v25, s23, v24
	v_bfe_u32 v25, v26, 16, 1
	v_lshl_add_u64 v[40:41], s[8:9], 0, v[36:37]
	v_add3_u32 v53, v54, v53, s22
	v_bfe_u32 v54, v55, 16, 1
	v_add3_u32 v25, v26, v25, s22
	v_bfe_u32 v26, v27, 16, 1
	v_lshrrev_b32_e32 v53, 16, v53
	v_add3_u32 v54, v55, v54, s22
	v_add_co_u32_e32 v56, vcc, s24, v40
	v_lshrrev_b32_e32 v25, 16, v25
	v_add3_u32 v26, v27, v26, s22
	v_and_or_b32 v53, v54, s23, v53
	v_addc_co_u32_e32 v57, vcc, 0, v41, vcc
	v_and_or_b32 v25, v26, s23, v25
	global_store_dwordx2 v[56:57], v[52:53], off nt
	global_store_dwordx2 v[56:57], v[24:25], off offset:512 nt
	ds_read_b128 v[24:27], v50 offset:2048
	ds_read_b128 v[28:31], v50 offset:10240
	v_pk_mul_f32 v[58:59], v[22:23], v[44:45] op_sel_hi:[1,0]
	v_pk_mul_f32 v[60:61], v[20:21], v[44:45] op_sel_hi:[1,0]
	ds_read_b128 v[20:23], v50 offset:3072
	ds_read_b128 v[52:55], v50 offset:11264
	v_pk_mul_f32 v[16:17], v[16:17], v[44:45] op_sel_hi:[1,0]
	s_waitcnt lgkmcnt(2)
	v_pk_fma_f32 v[24:25], v[60:61], v[24:25], v[28:29]
	v_pk_mul_f32 v[18:19], v[18:19], v[44:45] op_sel_hi:[1,0]
	v_bfe_u32 v28, v24, 16, 1
	s_waitcnt lgkmcnt(0)
	v_pk_fma_f32 v[16:17], v[16:17], v[20:21], v[52:53]
	v_add3_u32 v24, v24, v28, s22
	v_bfe_u32 v20, v16, 16, 1
	v_bfe_u32 v28, v25, 16, 1
	v_add3_u32 v16, v16, v20, s22
	v_bfe_u32 v20, v17, 16, 1
	v_pk_fma_f32 v[26:27], v[58:59], v[26:27], v[30:31]
	v_lshrrev_b32_e32 v24, 16, v24
	v_add3_u32 v25, v25, v28, s22
	v_pk_fma_f32 v[18:19], v[18:19], v[22:23], v[54:55]
	v_lshrrev_b32_e32 v16, 16, v16
	v_add3_u32 v17, v17, v20, s22
	v_and_or_b32 v24, v25, s23, v24
	v_bfe_u32 v25, v26, 16, 1
	v_and_or_b32 v16, v17, s23, v16
	v_bfe_u32 v17, v18, 16, 1
	v_add3_u32 v25, v26, v25, s22
	v_bfe_u32 v26, v27, 16, 1
	v_add3_u32 v17, v18, v17, s22
	v_bfe_u32 v18, v19, 16, 1
	v_lshrrev_b32_e32 v25, 16, v25
	v_add3_u32 v26, v27, v26, s22
	v_lshrrev_b32_e32 v17, 16, v17
	v_add3_u32 v18, v19, v18, s22
	v_and_or_b32 v25, v26, s23, v25
	v_and_or_b32 v17, v18, s23, v17
	global_store_dwordx2 v[56:57], v[24:25], off offset:1024 nt
	global_store_dwordx2 v[56:57], v[16:17], off offset:1536 nt
	ds_read_b128 v[16:19], v50 offset:4096
	ds_read_b128 v[20:23], v50 offset:12288
	v_pk_mul_f32 v[28:29], v[14:15], v[44:45] op_sel_hi:[1,0]
	v_pk_mul_f32 v[30:31], v[12:13], v[44:45] op_sel_hi:[1,0]
	ds_read_b128 v[12:15], v50 offset:5120
	ds_read_b128 v[24:27], v50 offset:13312
	v_pk_mul_f32 v[8:9], v[8:9], v[44:45] op_sel_hi:[1,0]
	s_waitcnt lgkmcnt(2)
	v_pk_fma_f32 v[16:17], v[30:31], v[16:17], v[20:21]
	v_pk_mul_f32 v[10:11], v[10:11], v[44:45] op_sel_hi:[1,0]
	v_bfe_u32 v20, v16, 16, 1
	s_waitcnt lgkmcnt(0)
	v_pk_fma_f32 v[8:9], v[8:9], v[12:13], v[24:25]
	v_add3_u32 v16, v16, v20, s22
	v_bfe_u32 v12, v8, 16, 1
	v_bfe_u32 v20, v17, 16, 1
	v_add3_u32 v8, v8, v12, s22
	v_bfe_u32 v12, v9, 16, 1
	v_pk_fma_f32 v[18:19], v[28:29], v[18:19], v[22:23]
	v_lshrrev_b32_e32 v16, 16, v16
	v_add3_u32 v17, v17, v20, s22
	v_pk_fma_f32 v[10:11], v[10:11], v[14:15], v[26:27]
	v_lshrrev_b32_e32 v8, 16, v8
	v_add3_u32 v9, v9, v12, s22
	v_and_or_b32 v16, v17, s23, v16
	v_bfe_u32 v17, v18, 16, 1
	v_and_or_b32 v8, v9, s23, v8
	v_bfe_u32 v9, v10, 16, 1
	v_add3_u32 v17, v18, v17, s22
	v_bfe_u32 v18, v19, 16, 1
	v_add3_u32 v9, v10, v9, s22
	v_bfe_u32 v10, v11, 16, 1
	v_lshrrev_b32_e32 v17, 16, v17
	v_add3_u32 v18, v19, v18, s22
	v_lshrrev_b32_e32 v9, 16, v9
	v_add3_u32 v10, v11, v10, s22
	v_and_or_b32 v17, v18, s23, v17
	v_and_or_b32 v9, v10, s23, v9
	global_store_dwordx2 v[56:57], v[16:17], off offset:2048 nt
	global_store_dwordx2 v[56:57], v[8:9], off offset:2560 nt
	ds_read_b128 v[8:11], v50 offset:6144
	ds_read_b128 v[12:15], v50 offset:14336
	v_pk_mul_f32 v[20:21], v[6:7], v[44:45] op_sel_hi:[1,0]
	v_pk_mul_f32 v[22:23], v[4:5], v[44:45] op_sel_hi:[1,0]
	ds_read_b128 v[4:7], v50 offset:7168
	ds_read_b128 v[16:19], v50 offset:15360
	v_pk_mul_f32 v[0:1], v[0:1], v[44:45] op_sel_hi:[1,0]
	s_waitcnt lgkmcnt(2)
	v_pk_fma_f32 v[8:9], v[22:23], v[8:9], v[12:13]
	v_pk_mul_f32 v[2:3], v[2:3], v[44:45] op_sel_hi:[1,0]
	v_bfe_u32 v12, v8, 16, 1
	s_waitcnt lgkmcnt(0)
; #define GAS __attribute__((address_space(1)))
; #define LAS __attribute__((address_space(3)))
; __device__ __forceinline__ float dot4(f32x4 a, f32x4 b) { return (a.x * b.x + a.y * b.y) + (a.z * b.z + a.w * b.w); }
; __device__ __forceinline__ u32x2 pack4(f32x4 v) { u32x2 w; w.x = pk2(v.x, v.y); w.y = pk2(v.z, v.w); return w; }
; __device__ __forceinline__ void phase8(KP kp, LAS unsigned char* lds, int wave, int bid) {
;     ...
;     for (int q = 0; q < 4; ++q) {
;         const int lt = 4 * wave + q, t = 32 * bid + lt;
;         const GAS f32x4* xr = (const GAS f32x4*)(X1 + (size_t)t * DM) + lane;
;         f32x4 v[8]; float s = 0.f;
; #pragma unroll
;         for (int j = 0; j < 8; ++j) { v[j] = xr[64 * j]; s += dot4(v[j], v[j]); }
;         const float rstd = 1.0f / sqrtf(wave_sum(s) * (1.0f / DM) + EPS);
;         if (lane == 0) rs[lt] = rstd;
;         GAS u32x2* o8 = (GAS u32x2*)(H + (size_t)t * DM) + lane;
; #pragma unroll
;         for (int j = 0; j < 8; ++j) { const f32x4 av = *(const LAS f32x4*)(A2 + 256 * j + 4 * lane), bv = *(const LAS f32x4*)(B2 + 256 * j + 4 * lane);
;             o8[64 * j] = pack4(v[j] * rstd * av + bv); }
	v_pk_fma_f32 v[0:1], v[0:1], v[4:5], v[16:17]
	v_add3_u32 v8, v8, v12, s22
	v_bfe_u32 v4, v0, 16, 1
	v_bfe_u32 v12, v9, 16, 1
	v_add3_u32 v0, v0, v4, s22
	v_bfe_u32 v4, v1, 16, 1
	v_pk_fma_f32 v[10:11], v[20:21], v[10:11], v[14:15]
	v_lshrrev_b32_e32 v8, 16, v8
	v_add3_u32 v9, v9, v12, s22
	v_pk_fma_f32 v[2:3], v[2:3], v[6:7], v[18:19]
	v_lshrrev_b32_e32 v0, 16, v0
	v_add3_u32 v1, v1, v4, s22
	v_and_or_b32 v8, v9, s23, v8
	v_bfe_u32 v9, v10, 16, 1
	v_and_or_b32 v0, v1, s23, v0
	v_bfe_u32 v1, v2, 16, 1
	v_add3_u32 v9, v10, v9, s22
	v_bfe_u32 v10, v11, 16, 1
	v_add3_u32 v1, v2, v1, s22
	v_bfe_u32 v2, v3, 16, 1
	v_lshrrev_b32_e32 v9, 16, v9
	v_add3_u32 v10, v11, v10, s22
	v_lshrrev_b32_e32 v1, 16, v1
	v_add3_u32 v2, v3, v2, s22
	v_and_or_b32 v9, v10, s23, v9
	v_and_or_b32 v1, v2, s23, v1
	v_add_co_u32_e32 v52, vcc, s28, v42
	global_store_dwordx2 v[56:57], v[8:9], off offset:3072 nt
	global_store_dwordx2 v[56:57], v[0:1], off offset:3584 nt
	v_addc_co_u32_e32 v53, vcc, 0, v43, vcc
	v_add_co_u32_e32 v42, vcc, s25, v42
	s_nop 1
	v_addc_co_u32_e32 v43, vcc, 0, v43, vcc
	s_waitcnt vmcnt(8)
	s_nop 1
	v_mov_b32_e32 v0, v160
	v_mov_b32_e32 v1, v161
	v_mov_b32_e32 v2, v162
	v_mov_b32_e32 v3, v163
	v_mov_b32_e32 v4, v164
	v_mov_b32_e32 v5, v165
	v_mov_b32_e32 v6, v166
	v_mov_b32_e32 v7, v167
	v_mov_b32_e32 v8, v168
	v_mov_b32_e32 v9, v169
	v_mov_b32_e32 v10, v170
	v_mov_b32_e32 v11, v171
	v_mov_b32_e32 v12, v172
	v_mov_b32_e32 v13, v173
	v_mov_b32_e32 v14, v174
	v_mov_b32_e32 v15, v175
	v_mov_b32_e32 v16, v176
	v_mov_b32_e32 v17, v177
	v_mov_b32_e32 v18, v178
	v_mov_b32_e32 v19, v179
	v_mov_b32_e32 v20, v180
	v_mov_b32_e32 v21, v181
	v_mov_b32_e32 v22, v182
	v_mov_b32_e32 v23, v183
	v_mov_b32_e32 v24, v184
	v_mov_b32_e32 v25, v185
	v_mov_b32_e32 v26, v186
	v_mov_b32_e32 v27, v187
	v_mov_b32_e32 v28, v188
	v_mov_b32_e32 v29, v189
	v_mov_b32_e32 v30, v190
	v_mov_b32_e32 v31, v191
	v_mul_f32_e32 v42, v29, v29
	v_mul_f32_e32 v43, v31, v31
	v_fmac_f32_e32 v42, v28, v28
	v_fmac_f32_e32 v43, v30, v30
	v_add_f32_e32 v42, v42, v43
	v_mul_f32_e32 v43, v25, v25
	v_mul_f32_e32 v44, v27, v27
	v_fmac_f32_e32 v43, v24, v24
	v_fmac_f32_e32 v44, v26, v26
	v_add_f32_e32 v43, v43, v44
	v_add_f32_e32 v42, v42, v43
	v_mul_f32_e32 v43, v21, v21
	v_mul_f32_e32 v44, v23, v23
	v_fmac_f32_e32 v43, v20, v20
	v_fmac_f32_e32 v44, v22, v22
	v_add_f32_e32 v43, v43, v44
	v_add_f32_e32 v42, v42, v43
	v_mul_f32_e32 v43, v17, v17
	v_mul_f32_e32 v44, v19, v19
	v_fmac_f32_e32 v43, v16, v16
	v_fmac_f32_e32 v44, v18, v18
	v_add_f32_e32 v43, v43, v44
	v_add_f32_e32 v42, v42, v43
	v_mul_f32_e32 v43, v13, v13
	v_mul_f32_e32 v44, v15, v15
	v_fmac_f32_e32 v43, v12, v12
	v_fmac_f32_e32 v44, v14, v14
	v_add_f32_e32 v43, v43, v44
	v_add_f32_e32 v42, v42, v43
	v_mul_f32_e32 v43, v9, v9
	v_mul_f32_e32 v44, v11, v11
	v_fmac_f32_e32 v43, v8, v8
	v_fmac_f32_e32 v44, v10, v10
	v_add_f32_e32 v43, v43, v44
	v_add_f32_e32 v42, v42, v43
	v_mul_f32_e32 v43, v5, v5
	v_mul_f32_e32 v44, v7, v7
	v_fmac_f32_e32 v43, v4, v4
	v_fmac_f32_e32 v44, v6, v6
	v_add_f32_e32 v43, v43, v44
	v_add_f32_e32 v42, v42, v43
	v_mul_f32_e32 v43, v1, v1
	v_mul_f32_e32 v44, v3, v3
	v_fmac_f32_e32 v43, v0, v0
	v_fmac_f32_e32 v44, v2, v2
	v_add_f32_e32 v43, v43, v44
	v_add_f32_e32 v42, v42, v43
	s_nop 1
	v_add_f32_dpp v42, v42, v42 quad_perm:[1,0,3,2] row_mask:0xf bank_mask:0xf
	s_nop 1
	v_add_f32_dpp v42, v42, v42 quad_perm:[2,3,0,1] row_mask:0xf bank_mask:0xf
	s_nop 1
	v_add_f32_dpp v42, v42, v42 row_half_mirror row_mask:0xf bank_mask:0xf
	s_nop 1
	v_add_f32_dpp v42, v42, v42 row_mirror row_mask:0xf bank_mask:0xf
	v_mov_b32_e32 v43, v42
	s_nop 1
	v_permlane16_swap_b32_e32 v42, v43
	v_add_f32_e32 v42, v42, v43
	v_mov_b32_e32 v43, v42
	s_nop 1
	v_permlane32_swap_b32_e32 v42, v43
	v_add_f32_e32 v42, v42, v43
	v_fmamk_f32 v42, v42, 0x3a000000, v35
	v_mul_f32_e32 v43, 0x4f800000, v42
	v_cmp_gt_f32_e32 vcc, s21, v42
	s_nop 1
	v_cndmask_b32_e32 v42, v42, v43, vcc
	v_sqrt_f32_e32 v43, v42
	s_nop 0
	v_add_u32_e32 v44, -1, v43
	v_fma_f32 v52, -v44, v43, v42
	v_cmp_ge_f32_e64 s[6:7], 0, v52
	v_add_u32_e32 v52, 1, v43
	s_nop 0
	v_cndmask_b32_e64 v44, v43, v44, s[6:7]
	v_fma_f32 v43, -v52, v43, v42
	v_cmp_lt_f32_e64 s[6:7], 0, v43
	s_nop 1
	v_cndmask_b32_e64 v43, v44, v52, s[6:7]
	v_mul_f32_e32 v44, 0x37800000, v43
	v_cndmask_b32_e32 v43, v43, v44, vcc
	v_cmp_class_f32_e32 vcc, v42, v51
	s_nop 1
	v_cndmask_b32_e32 v42, v43, v42, vcc
	v_div_scale_f32 v43, s[6:7], v42, v42, 1.0
	v_rcp_f32_e32 v44, v43
	s_nop 0
	v_fma_f32 v52, -v43, v44, 1.0
	v_fmac_f32_e32 v44, v52, v44
	v_div_scale_f32 v52, vcc, 1.0, v42, 1.0
	v_mul_f32_e32 v53, v52, v44
	v_fma_f32 v54, -v43, v53, v52
	v_fmac_f32_e32 v53, v54, v44
	v_fma_f32 v43, -v43, v53, v52
	v_div_fmas_f32 v43, v43, v44, v53
	v_div_fixup_f32 v42, v43, v42, 1.0
	s_and_saveexec_b64 s[6:7], s[2:3]
	s_cbranch_execz .LBB0_932
	s_add_i32 s4, s5, s18
	v_mov_b32_e32 v43, s4
	ds_write_b32 v43, v42 offset:4
	s_branch .LBB0_932
